# MoE down GEMM: compiler-inserted vmcnt(0) at the K-loop head (guarding a stale epilogue load) moved out of the loop, so the staged LDS-DMA pipeline is no longer drained every K iteration
# speedup vs baseline: 1.0284x; 1.0007x over previous
; #define PG8_STAGE(bufoff, goff, voff) do { _Pragma("unroll") for (int _i = 0; _i < 2; ++_i) \
;         __builtin_amdgcn_raw_ptr_buffer_load_lds(rsrc, (PG8_LAS void*)(lds + (bufoff) + ldsw + _i * 8192), 16, (int)(voff), (int)((goff) + _i * p1##voff), 0, 0); } while (0)
; #define PG8_LDA(dst, b, h) do { _Pragma("unroll") for (int m = 0; m < 4; ++m) dst[m] = PG8_LD8(lds + PG8_SA(b, h) + aoff + m * 2048); } while (0)
; #define PG8_LDB(dst, b, h) do { _Pragma("unroll") for (int n = 0; n < 2; ++n) dst[n] = PG8_LD8(lds + PG8_SB(b, h) + boff + n * 2048); } while (0)
; #define PG8_WAIT_V(n) asm volatile("s_waitcnt vmcnt(" #n ")" ::: "memory")
; #define PG8_WAIT_L(n) asm volatile("s_waitcnt lgkmcnt(" #n ")" ::: "memory")
; #define PG8_BAR __builtin_amdgcn_s_barrier()
; #define PG8_SCHED __builtin_amdgcn_sched_barrier(0)
; #define PG8_ZERO() do { _Pragma("unroll") for (int a = 0; a < 2; ++a) _Pragma("unroll") for (int b = 0; b < 2; ++b) _Pragma("unroll") for (int m = 0; m < 4; ++m) _Pragma("unroll") for (int n = 0; n < 2; ++n) acc[a][b][m][n] = (f32x4){0.f, 0.f, 0.f, 0.f}; } while (0)
; template <class Epi, class Sched, bool ALIGN_EPI, bool F8 = false, int F8SC = F8_SCALES>
; __device__ __forceinline__ void gemm_phase(PG8_LAS unsigned char* lds, const __amdgpu_buffer_rsrc_t rsrc, const int lda, const int ldb, const int K, const Sched& S, const Epi& E) {
;     ...
;         for (int t = 0; t < nt; t += 2) {
;             const bool last = (t == nt - 2);
;             const unsigned a1 = cA + (unsigned)(t + 1) * kstep;
;             const unsigned a2 = last ? nA : cA + (unsigned)(t + 2) * kstep, b2 = last ? nB : cB + (unsigned)(t + 2) * kstep;
;             const unsigned a3 = a2 + kstep, b3 = b2 + kstep;
;             PG8_LDB(B0, 0, 0); PG8_LDB(B1, 0, 1); PG8_SCHED; PG8_LDA(At, 0, 0); PG8_STAGE(PG8_SA(1, 1), a1 + hsA, voffA);
;             PG8_WAIT_V(8); PG8_WAIT_L(0); PG8_BAR; PG8_MMA(0, 0, At, B0); PG8_MMA(0, 1, At, B1); PG8_BAR; PG8_SCHED;
;     ...
;         if (!keep) PG8_ZERO();
.LBB0_1724:
	v_mov_b32_e32 v2, 0
	s_add_i32 s4, s50, 0x60080
	s_add_i32 s5, s49, 0x100
	s_mov_b32 s49, -2
	v_mov_b32_e32 v3, v2
	v_mov_b32_e32 v4, v2
	v_mov_b32_e32 v5, v2
	v_mov_b32_e32 v6, v2
	v_mov_b32_e32 v7, v2
	v_mov_b32_e32 v8, v2
	v_mov_b32_e32 v9, v2
	s_waitcnt vmcnt(25)
	v_mov_b32_e32 v18, v2
	v_mov_b32_e32 v19, v2
	v_mov_b32_e32 v20, v2
	v_mov_b32_e32 v21, v2
	s_waitcnt vmcnt(24)
	v_mov_b32_e32 v22, v2
	v_mov_b32_e32 v23, v2
	v_mov_b32_e32 v24, v2
	v_mov_b32_e32 v25, v2
	s_waitcnt vmcnt(21)
	v_mov_b32_e32 v34, v2
	v_mov_b32_e32 v35, v2
	v_mov_b32_e32 v36, v2
	v_mov_b32_e32 v37, v2
	s_waitcnt vmcnt(20)
	v_mov_b32_e32 v38, v2
	v_mov_b32_e32 v39, v2
	v_mov_b32_e32 v40, v2
	v_mov_b32_e32 v41, v2
	s_waitcnt vmcnt(17)
	v_mov_b32_e32 v50, v2
	v_mov_b32_e32 v51, v2
	v_mov_b32_e32 v52, v2
	v_mov_b32_e32 v53, v2
	s_waitcnt vmcnt(16)
	v_mov_b32_e32 v54, v2
	v_mov_b32_e32 v55, v2
	v_mov_b32_e32 v56, v2
	v_mov_b32_e32 v57, v2
	v_mov_b32_e32 v10, v2
	v_mov_b32_e32 v11, v2
	v_mov_b32_e32 v12, v2
	v_mov_b32_e32 v13, v2
	v_mov_b32_e32 v14, v2
	v_mov_b32_e32 v15, v2
	v_mov_b32_e32 v16, v2
	v_mov_b32_e32 v17, v2
	v_mov_b32_e32 v26, v2
	v_mov_b32_e32 v27, v2
	v_mov_b32_e32 v28, v2
	v_mov_b32_e32 v29, v2
	v_mov_b32_e32 v30, v2
	v_mov_b32_e32 v31, v2
	v_mov_b32_e32 v32, v2
	v_mov_b32_e32 v33, v2
	v_mov_b32_e32 v42, v2
	v_mov_b32_e32 v43, v2
	v_mov_b32_e32 v44, v2
	v_mov_b32_e32 v45, v2
	v_mov_b32_e32 v46, v2
	v_mov_b32_e32 v47, v2
	v_mov_b32_e32 v48, v2
	v_mov_b32_e32 v49, v2
	s_waitcnt vmcnt(15)
	v_mov_b32_e32 v58, v2
	v_mov_b32_e32 v59, v2
	v_mov_b32_e32 v60, v2
	v_mov_b32_e32 v61, v2
	s_waitcnt vmcnt(14)
	v_mov_b32_e32 v62, v2
	v_mov_b32_e32 v63, v2
	v_mov_b32_e32 v64, v2
	v_mov_b32_e32 v65, v2
	v_mov_b32_e32 v66, v2
	v_mov_b32_e32 v67, v2
	v_mov_b32_e32 v68, v2
	v_mov_b32_e32 v69, v2
	v_mov_b32_e32 v70, v2
	v_mov_b32_e32 v71, v2
	v_mov_b32_e32 v72, v2
	v_mov_b32_e32 v73, v2
	v_mov_b32_e32 v82, v2
	v_mov_b32_e32 v83, v2
	v_mov_b32_e32 v84, v2
	v_mov_b32_e32 v85, v2
	v_mov_b32_e32 v86, v2
	v_mov_b32_e32 v87, v2
	v_mov_b32_e32 v88, v2
	v_mov_b32_e32 v89, v2
	v_mov_b32_e32 v98, v2
	v_mov_b32_e32 v99, v2
	v_mov_b32_e32 v100, v2
	v_mov_b32_e32 v101, v2
	v_mov_b32_e32 v102, v2
	v_mov_b32_e32 v103, v2
	v_mov_b32_e32 v104, v2
	v_mov_b32_e32 v105, v2
	v_mov_b32_e32 v114, v2
	v_mov_b32_e32 v115, v2
	v_mov_b32_e32 v116, v2
	v_mov_b32_e32 v117, v2
	v_mov_b32_e32 v118, v2
	v_mov_b32_e32 v119, v2
	v_mov_b32_e32 v120, v2
	v_mov_b32_e32 v121, v2
	v_mov_b32_e32 v74, v2
	v_mov_b32_e32 v75, v2
	v_mov_b32_e32 v76, v2
	v_mov_b32_e32 v77, v2
	v_mov_b32_e32 v78, v2
	v_mov_b32_e32 v79, v2
	v_mov_b32_e32 v80, v2
	v_mov_b32_e32 v81, v2
	v_mov_b32_e32 v90, v2
	v_mov_b32_e32 v91, v2
	v_mov_b32_e32 v92, v2
	v_mov_b32_e32 v93, v2
	v_mov_b32_e32 v94, v2
	v_mov_b32_e32 v95, v2
	v_mov_b32_e32 v96, v2
	v_mov_b32_e32 v97, v2
	v_mov_b32_e32 v106, v2
	v_mov_b32_e32 v107, v2
	v_mov_b32_e32 v108, v2
	v_mov_b32_e32 v109, v2
	v_mov_b32_e32 v110, v2
	v_mov_b32_e32 v111, v2
	v_mov_b32_e32 v112, v2
	v_mov_b32_e32 v113, v2
	v_mov_b32_e32 v122, v2
	v_mov_b32_e32 v123, v2
	v_mov_b32_e32 v124, v2
	v_mov_b32_e32 v125, v2
	v_mov_b32_e32 v126, v2
	v_mov_b32_e32 v127, v2
	v_mov_b32_e32 v128, v2
	v_mov_b32_e32 v129, v2
	s_waitcnt vmcnt(0)
.LBB0_1725:
	ds_read_b128 v[130:133], v169
	ds_read_b128 v[134:137], v169 offset:1024
	ds_read_b128 v[138:141], v169 offset:2048
	ds_read_b128 v[142:145], v169 offset:3072
	ds_read_b128 v[150:153], v170
	ds_read_b128 v[154:157], v170 offset:1024
	ds_read_b128 v[158:161], v170 offset:2048
	ds_read_b128 v[162:165], v170 offset:3072
	s_add_i32 s50, s4, 0xfffa0080
	s_cmp_eq_u32 s49, 12
	s_cselect_b32 s50, s47, s50
	s_cselect_b32 s52, s46, s5
	s_add_i32 s51, s50, 0x80
	s_add_i32 s53, s4, 0xfffe0000
	s_mov_b32 s80, s96
	s_mov_b32 m0, s30
	ds_read_b128 v[176:179], v171
	ds_read_b128 v[180:183], v171 offset:1024
	ds_read_b128 v[184:187], v171 offset:2048
	ds_read_b128 v[188:191], v171 offset:3072
	ds_read_b128 v[192:195], v171 offset:4096
	ds_read_b128 v[196:199], v171 offset:5120
	ds_read_b128 v[200:203], v171 offset:6144
	ds_read_b128 v[204:207], v171 offset:7168
	buffer_load_dwordx4 v1, s[80:83], s53 offen lds
	s_mov_b32 m0, s31
	s_nop 0
	buffer_load_dwordx4 v1, s[80:83], s4 offen lds
	s_waitcnt vmcnt(8)
	s_waitcnt lgkmcnt(0)
	s_barrier
	s_setprio 1
	s_waitcnt lgkmcnt(6)
	v_mfma_scale_f32_16x16x128_f8f6f4 v[126:129], v[130:137], v[176:183], v[126:129], v172, v172 op_sel:[0,1,0] op_sel_hi:[0,0,0]
	v_mfma_scale_f32_16x16x128_f8f6f4 v[122:125], v[138:145], v[176:183], v[122:125], v172, v172 op_sel:[0,1,0] op_sel_hi:[0,0,0]
	s_waitcnt lgkmcnt(4)
	v_mfma_scale_f32_16x16x128_f8f6f4 v[110:113], v[130:137], v[184:191], v[110:113], v172, v172 op_sel:[0,1,0] op_sel_hi:[0,0,0]
	v_mfma_scale_f32_16x16x128_f8f6f4 v[106:109], v[138:145], v[184:191], v[106:109], v172, v172 op_sel:[0,1,0] op_sel_hi:[0,0,0]
	s_waitcnt lgkmcnt(2)
	v_mfma_scale_f32_16x16x128_f8f6f4 v[208:211], v[130:137], v[192:199], v[94:97], v172, v172 op_sel:[0,1,0] op_sel_hi:[0,0,0]
	v_mfma_scale_f32_16x16x128_f8f6f4 v[212:215], v[138:145], v[192:199], v[90:93], v172, v172 op_sel:[0,1,0] op_sel_hi:[0,0,0]
	s_waitcnt lgkmcnt(0)
	v_mfma_scale_f32_16x16x128_f8f6f4 v[216:219], v[130:137], v[200:207], v[78:81], v172, v172 op_sel:[0,1,0] op_sel_hi:[0,0,0]
	v_mfma_scale_f32_16x16x128_f8f6f4 v[220:223], v[138:145], v[200:207], v[74:77], v172, v172 op_sel:[0,1,0] op_sel_hi:[0,0,0]
	s_setprio 0
	s_setprio 1
	v_mfma_scale_f32_16x16x128_f8f6f4 v[118:121], v[150:157], v[176:183], v[118:121], v172, v172 op_sel:[0,1,0] op_sel_hi:[0,0,0]
	v_mfma_scale_f32_16x16x128_f8f6f4 v[114:117], v[158:165], v[176:183], v[114:117], v172, v172 op_sel:[0,1,0] op_sel_hi:[0,0,0]
	v_mfma_scale_f32_16x16x128_f8f6f4 v[102:105], v[150:157], v[184:191], v[102:105], v172, v172 op_sel:[0,1,0] op_sel_hi:[0,0,0]
	v_mfma_scale_f32_16x16x128_f8f6f4 v[98:101], v[158:165], v[184:191], v[98:101], v172, v172 op_sel:[0,1,0] op_sel_hi:[0,0,0]
	v_mfma_scale_f32_16x16x128_f8f6f4 v[176:179], v[150:157], v[192:199], v[86:89], v172, v172 op_sel:[0,1,0] op_sel_hi:[0,0,0]
	v_mfma_scale_f32_16x16x128_f8f6f4 v[180:183], v[158:165], v[192:199], v[82:85], v172, v172 op_sel:[0,1,0] op_sel_hi:[0,0,0]
	v_mfma_scale_f32_16x16x128_f8f6f4 v[184:187], v[150:157], v[200:207], v[70:73], v172, v172 op_sel:[0,1,0] op_sel_hi:[0,0,0]
	v_mfma_scale_f32_16x16x128_f8f6f4 v[188:191], v[158:165], v[200:207], v[66:69], v172, v172 op_sel:[0,1,0] op_sel_hi:[0,0,0]
	s_setprio 0
	s_barrier
; #define PG8_STAGE(bufoff, goff, voff) do { _Pragma("unroll") for (int _i = 0; _i < 2; ++_i) \
;         __builtin_amdgcn_raw_ptr_buffer_load_lds(rsrc, (PG8_LAS void*)(lds + (bufoff) + ldsw + _i * 8192), 16, (int)(voff), (int)((goff) + _i * p1##voff), 0, 0); } while (0)
; #define PG8_LDA(dst, b, h) do { _Pragma("unroll") for (int m = 0; m < 4; ++m) dst[m] = PG8_LD8(lds + PG8_SA(b, h) + aoff + m * 2048); } while (0)
; #define PG8_LDB(dst, b, h) do { _Pragma("unroll") for (int n = 0; n < 2; ++n) dst[n] = PG8_LD8(lds + PG8_SB(b, h) + boff + n * 2048); } while (0)
; #define PG8_WAIT_V(n) asm volatile("s_waitcnt vmcnt(" #n ")" ::: "memory")
; #define PG8_WAIT_L(n) asm volatile("s_waitcnt lgkmcnt(" #n ")" ::: "memory")
; #define PG8_BAR __builtin_amdgcn_s_barrier()
; #define PG8_SCHED __builtin_amdgcn_sched_barrier(0)
; template <class Epi, class Sched, bool ALIGN_EPI, bool F8 = false, int F8SC = F8_SCALES>
; __device__ __forceinline__ void gemm_phase(PG8_LAS unsigned char* lds, const __amdgpu_buffer_rsrc_t rsrc, const int lda, const int ldb, const int K, const Sched& S, const Epi& E) {
;     ...
;             PG8_LDA(At, 0, 1); PG8_STAGE(PG8_SB(0, 0), b2, voffB); PG8_STAGE(PG8_SB(0, 1), b2 + hsB, voffB); PG8_STAGE(PG8_SA(0, 0), a2, voffA);
;             PG8_WAIT_V(8); PG8_WAIT_L(0); PG8_BAR; PG8_MMA(1, 0, At, B0); PG8_MMA(1, 1, At, B1); PG8_BAR; PG8_SCHED;
;             PG8_LDB(B0, 1, 0); PG8_LDB(B1, 1, 1); PG8_SCHED; PG8_LDA(At, 1, 0); PG8_STAGE(PG8_SA(0, 1), a2 + hsA, voffA);
	s_mov_b32 m0, s16
	s_nop 3
	ds_read_b128 v[66:69], v171 offset:16384
	ds_read_b128 v[70:73], v171 offset:17408
	ds_read_b128 v[74:77], v171 offset:18432
	ds_read_b128 v[78:81], v171 offset:19456
	ds_read_b128 v[82:85], v171 offset:20480
	ds_read_b128 v[86:89], v171 offset:21504
	ds_read_b128 v[90:93], v171 offset:22528
	ds_read_b128 v[94:97], v171 offset:23552
	buffer_load_dwordx4 v168, s[80:83], s52 offen lds
	s_add_i32 s53, s52, 0x20000
	s_mov_b32 m0, s17
	s_nop 0
	buffer_load_dwordx4 v168, s[80:83], s53 offen lds
	s_add_i32 s53, s52, 0x40000
	s_mov_b32 m0, s18
	s_nop 0
	buffer_load_dwordx4 v168, s[80:83], s53 offen lds
	s_add_i32 s53, s52, 0x60000
	s_mov_b32 m0, s19
	s_nop 0
	buffer_load_dwordx4 v168, s[80:83], s53 offen lds
	s_mov_b32 m0, s15
	s_add_i32 s53, s50, 0x20000
	buffer_load_dwordx4 v1, s[80:83], s50 offen lds
	s_mov_b32 m0, s20
	s_nop 0
	buffer_load_dwordx4 v1, s[80:83], s53 offen lds
	s_waitcnt vmcnt(8)
	s_waitcnt lgkmcnt(0)
	s_barrier
	s_setprio 1
	s_waitcnt lgkmcnt(6)
	v_mfma_scale_f32_16x16x128_f8f6f4 v[62:65], v[130:137], v[66:73], v[62:65], v172, v172 op_sel:[0,1,0] op_sel_hi:[0,0,0]
	v_mfma_scale_f32_16x16x128_f8f6f4 v[58:61], v[138:145], v[66:73], v[58:61], v172, v172 op_sel:[0,1,0] op_sel_hi:[0,0,0]
	s_waitcnt lgkmcnt(4)
	v_mfma_scale_f32_16x16x128_f8f6f4 v[192:195], v[130:137], v[74:81], v[46:49], v172, v172 op_sel:[0,1,0] op_sel_hi:[0,0,0]
	v_mfma_scale_f32_16x16x128_f8f6f4 v[196:199], v[138:145], v[74:81], v[42:45], v172, v172 op_sel:[0,1,0] op_sel_hi:[0,0,0]
	s_waitcnt lgkmcnt(2)
	v_mfma_scale_f32_16x16x128_f8f6f4 v[200:203], v[130:137], v[82:89], v[30:33], v172, v172 op_sel:[0,1,0] op_sel_hi:[0,0,0]
	v_mfma_scale_f32_16x16x128_f8f6f4 v[204:207], v[138:145], v[82:89], v[26:29], v172, v172 op_sel:[0,1,0] op_sel_hi:[0,0,0]
	s_waitcnt lgkmcnt(0)
	v_mfma_scale_f32_16x16x128_f8f6f4 v[224:227], v[130:137], v[90:97], v[14:17], v172, v172 op_sel:[0,1,0] op_sel_hi:[0,0,0]
	v_mfma_scale_f32_16x16x128_f8f6f4 v[228:231], v[138:145], v[90:97], v[10:13], v172, v172 op_sel:[0,1,0] op_sel_hi:[0,0,0]
	s_setprio 0
	s_setprio 1
	v_mfma_scale_f32_16x16x128_f8f6f4 v[54:57], v[150:157], v[66:73], v[54:57], v172, v172 op_sel:[0,1,0] op_sel_hi:[0,0,0]
	v_mfma_scale_f32_16x16x128_f8f6f4 v[50:53], v[158:165], v[66:73], v[50:53], v172, v172 op_sel:[0,1,0] op_sel_hi:[0,0,0]
	v_mfma_scale_f32_16x16x128_f8f6f4 v[232:235], v[150:157], v[74:81], v[38:41], v172, v172 op_sel:[0,1,0] op_sel_hi:[0,0,0]
	v_mfma_scale_f32_16x16x128_f8f6f4 v[236:239], v[158:165], v[74:81], v[34:37], v172, v172 op_sel:[0,1,0] op_sel_hi:[0,0,0]
	v_mfma_scale_f32_16x16x128_f8f6f4 v[240:243], v[150:157], v[82:89], v[22:25], v172, v172 op_sel:[0,1,0] op_sel_hi:[0,0,0]
	v_mfma_scale_f32_16x16x128_f8f6f4 v[244:247], v[158:165], v[82:89], v[18:21], v172, v172 op_sel:[0,1,0] op_sel_hi:[0,0,0]
	v_mfma_scale_f32_16x16x128_f8f6f4 v[248:251], v[150:157], v[90:97], v[6:9], v172, v172 op_sel:[0,1,0] op_sel_hi:[0,0,0]
	v_mfma_scale_f32_16x16x128_f8f6f4 v[146:149], v[158:165], v[90:97], v[2:5], v172, v172 op_sel:[0,1,0] op_sel_hi:[0,0,0]
	s_setprio 0
	s_barrier
	s_nop 4
	ds_read_b128 v[2:5], v173
	ds_read_b128 v[6:9], v173 offset:1024
	ds_read_b128 v[18:21], v173 offset:2048
	ds_read_b128 v[22:25], v173 offset:3072
	ds_read_b128 v[130:133], v174
	ds_read_b128 v[134:137], v174 offset:1024
	ds_read_b128 v[138:141], v174 offset:2048
	ds_read_b128 v[142:145], v174 offset:3072
	s_mov_b32 m0, s21
	s_add_i32 s53, s50, 0x40000
	ds_read_b128 v[10:13], v171 offset:32768
	ds_read_b128 v[14:17], v171 offset:33792
	ds_read_b128 v[26:29], v171 offset:34816
	ds_read_b128 v[30:33], v171 offset:35840
	ds_read_b128 v[34:37], v171 offset:36864
	ds_read_b128 v[38:41], v171 offset:37888
	ds_read_b128 v[42:45], v171 offset:38912
	ds_read_b128 v[46:49], v171 offset:39936
	buffer_load_dwordx4 v1, s[80:83], s53 offen lds
	s_add_i32 s53, s50, 0x60000
	s_mov_b32 m0, s22
	s_nop 0
	buffer_load_dwordx4 v1, s[80:83], s53 offen lds
	s_waitcnt vmcnt(8)
	s_waitcnt lgkmcnt(0)
	s_barrier
; #define PG8_STAGE(bufoff, goff, voff) do { _Pragma("unroll") for (int _i = 0; _i < 2; ++_i) \
;         __builtin_amdgcn_raw_ptr_buffer_load_lds(rsrc, (PG8_LAS void*)(lds + (bufoff) + ldsw + _i * 8192), 16, (int)(voff), (int)((goff) + _i * p1##voff), 0, 0); } while (0)
; #define PG8_LDA(dst, b, h) do { _Pragma("unroll") for (int m = 0; m < 4; ++m) dst[m] = PG8_LD8(lds + PG8_SA(b, h) + aoff + m * 2048); } while (0)
; #define PG8_LDB(dst, b, h) do { _Pragma("unroll") for (int n = 0; n < 2; ++n) dst[n] = PG8_LD8(lds + PG8_SB(b, h) + boff + n * 2048); } while (0)
; #define PG8_WAIT_V(n) asm volatile("s_waitcnt vmcnt(" #n ")" ::: "memory")
; #define PG8_WAIT_L(n) asm volatile("s_waitcnt lgkmcnt(" #n ")" ::: "memory")
; #define PG8_BAR __builtin_amdgcn_s_barrier()
; #define PG8_SCHED __builtin_amdgcn_sched_barrier(0)
; template <class Epi, class Sched, bool ALIGN_EPI, bool F8 = false, int F8SC = F8_SCALES>
; __device__ __forceinline__ void gemm_phase(PG8_LAS unsigned char* lds, const __amdgpu_buffer_rsrc_t rsrc, const int lda, const int ldb, const int K, const Sched& S, const Epi& E) {
;     ...
;             PG8_LDB(B0, 1, 0); PG8_LDB(B1, 1, 1); PG8_SCHED; PG8_LDA(At, 1, 0); PG8_STAGE(PG8_SA(0, 1), a2 + hsA, voffA);
;             PG8_WAIT_V(8); PG8_WAIT_L(0); PG8_BAR; PG8_MMA(0, 0, At, B0); PG8_MMA(0, 1, At, B1); PG8_BAR; PG8_SCHED;
;             PG8_LDA(At, 1, 1); PG8_STAGE(PG8_SB(1, 0), b3, voffB); PG8_STAGE(PG8_SB(1, 1), b3 + hsB, voffB); PG8_STAGE(PG8_SA(1, 0), a3, voffA);
;             PG8_WAIT_V(8); PG8_WAIT_L(0); PG8_BAR; PG8_MMA(1, 0, At, B0); PG8_MMA(1, 1, At, B1); PG8_BAR; PG8_SCHED;
;         }
;         if constexpr (ALIGN_EPI) { if (wr == 0) PG8_BAR; }
	s_setprio 1
	s_waitcnt lgkmcnt(6)
	v_mfma_scale_f32_16x16x128_f8f6f4 v[126:129], v[2:9], v[10:17], v[126:129], v172, v172 op_sel:[0,1,0] op_sel_hi:[0,0,0]
	v_mfma_scale_f32_16x16x128_f8f6f4 v[122:125], v[18:25], v[10:17], v[122:125], v172, v172 op_sel:[0,1,0] op_sel_hi:[0,0,0]
	s_waitcnt lgkmcnt(4)
	v_mfma_scale_f32_16x16x128_f8f6f4 v[110:113], v[2:9], v[26:33], v[110:113], v172, v172 op_sel:[0,1,0] op_sel_hi:[0,0,0]
	v_mfma_scale_f32_16x16x128_f8f6f4 v[106:109], v[18:25], v[26:33], v[106:109], v172, v172 op_sel:[0,1,0] op_sel_hi:[0,0,0]
	s_waitcnt lgkmcnt(2)
	v_mfma_scale_f32_16x16x128_f8f6f4 v[94:97], v[2:9], v[34:41], v[208:211], v172, v172 op_sel:[0,1,0] op_sel_hi:[0,0,0]
	v_mfma_scale_f32_16x16x128_f8f6f4 v[90:93], v[18:25], v[34:41], v[212:215], v172, v172 op_sel:[0,1,0] op_sel_hi:[0,0,0]
	s_waitcnt lgkmcnt(0)
	v_mfma_scale_f32_16x16x128_f8f6f4 v[78:81], v[2:9], v[42:49], v[216:219], v172, v172 op_sel:[0,1,0] op_sel_hi:[0,0,0]
	v_mfma_scale_f32_16x16x128_f8f6f4 v[74:77], v[18:25], v[42:49], v[220:223], v172, v172 op_sel:[0,1,0] op_sel_hi:[0,0,0]
	s_setprio 0
	s_setprio 1
	v_mfma_scale_f32_16x16x128_f8f6f4 v[118:121], v[130:137], v[10:17], v[118:121], v172, v172 op_sel:[0,1,0] op_sel_hi:[0,0,0]
	v_mfma_scale_f32_16x16x128_f8f6f4 v[114:117], v[138:145], v[10:17], v[114:117], v172, v172 op_sel:[0,1,0] op_sel_hi:[0,0,0]
	v_mfma_scale_f32_16x16x128_f8f6f4 v[102:105], v[130:137], v[26:33], v[102:105], v172, v172 op_sel:[0,1,0] op_sel_hi:[0,0,0]
	v_mfma_scale_f32_16x16x128_f8f6f4 v[98:101], v[138:145], v[26:33], v[98:101], v172, v172 op_sel:[0,1,0] op_sel_hi:[0,0,0]
	v_mfma_scale_f32_16x16x128_f8f6f4 v[86:89], v[130:137], v[34:41], v[176:179], v172, v172 op_sel:[0,1,0] op_sel_hi:[0,0,0]
	v_mfma_scale_f32_16x16x128_f8f6f4 v[82:85], v[138:145], v[34:41], v[180:183], v172, v172 op_sel:[0,1,0] op_sel_hi:[0,0,0]
	v_mfma_scale_f32_16x16x128_f8f6f4 v[70:73], v[130:137], v[42:49], v[184:187], v172, v172 op_sel:[0,1,0] op_sel_hi:[0,0,0]
	v_mfma_scale_f32_16x16x128_f8f6f4 v[66:69], v[138:145], v[42:49], v[188:191], v172, v172 op_sel:[0,1,0] op_sel_hi:[0,0,0]
	s_setprio 0
	s_barrier
	s_mov_b32 m0, s24
	s_add_i32 s53, s52, 0x80
	ds_read_b128 v[34:37], v171 offset:49152
	ds_read_b128 v[38:41], v171 offset:50176
	ds_read_b128 v[150:153], v171 offset:51200
	ds_read_b128 v[154:157], v171 offset:52224
	ds_read_b128 v[158:161], v171 offset:53248
	ds_read_b128 v[162:165], v171 offset:54272
	ds_read_b128 v[176:179], v171 offset:55296
	ds_read_b128 v[180:183], v171 offset:56320
	buffer_load_dwordx4 v168, s[80:83], s53 offen lds
	s_add_i32 s53, s52, 0x20080
	s_mov_b32 m0, s25
	s_add_i32 s50, s50, 0x20080
	buffer_load_dwordx4 v168, s[80:83], s53 offen lds
	s_add_i32 s53, s52, 0x40080
	s_mov_b32 m0, s28
	s_add_i32 s52, s52, 0x60080
	buffer_load_dwordx4 v168, s[80:83], s53 offen lds
	s_mov_b32 m0, s29
	s_nop 0
	buffer_load_dwordx4 v168, s[80:83], s52 offen lds
	s_mov_b32 m0, s26
	s_nop 0
	buffer_load_dwordx4 v1, s[80:83], s51 offen lds
	s_mov_b32 m0, s27
	s_nop 0
	buffer_load_dwordx4 v1, s[80:83], s50 offen lds
	s_waitcnt vmcnt(8)
	s_waitcnt lgkmcnt(0)
	s_barrier
	s_setprio 1
	s_waitcnt lgkmcnt(6)
	v_mfma_scale_f32_16x16x128_f8f6f4 v[62:65], v[2:9], v[34:41], v[62:65], v172, v172 op_sel:[0,1,0] op_sel_hi:[0,0,0]
	v_mfma_scale_f32_16x16x128_f8f6f4 v[58:61], v[18:25], v[34:41], v[58:61], v172, v172 op_sel:[0,1,0] op_sel_hi:[0,0,0]
	s_waitcnt lgkmcnt(4)
	v_mfma_scale_f32_16x16x128_f8f6f4 v[46:49], v[2:9], v[150:157], v[192:195], v172, v172 op_sel:[0,1,0] op_sel_hi:[0,0,0]
	v_mfma_scale_f32_16x16x128_f8f6f4 v[42:45], v[18:25], v[150:157], v[196:199], v172, v172 op_sel:[0,1,0] op_sel_hi:[0,0,0]
	s_waitcnt lgkmcnt(2)
	v_mfma_scale_f32_16x16x128_f8f6f4 v[30:33], v[2:9], v[158:165], v[200:203], v172, v172 op_sel:[0,1,0] op_sel_hi:[0,0,0]
	v_mfma_scale_f32_16x16x128_f8f6f4 v[26:29], v[18:25], v[158:165], v[204:207], v172, v172 op_sel:[0,1,0] op_sel_hi:[0,0,0]
	s_waitcnt lgkmcnt(0)
	v_mfma_scale_f32_16x16x128_f8f6f4 v[14:17], v[2:9], v[176:183], v[224:227], v172, v172 op_sel:[0,1,0] op_sel_hi:[0,0,0]
	v_mfma_scale_f32_16x16x128_f8f6f4 v[10:13], v[18:25], v[176:183], v[228:231], v172, v172 op_sel:[0,1,0] op_sel_hi:[0,0,0]
	s_setprio 0
	s_setprio 1
	v_mfma_scale_f32_16x16x128_f8f6f4 v[54:57], v[130:137], v[34:41], v[54:57], v172, v172 op_sel:[0,1,0] op_sel_hi:[0,0,0]
	v_mfma_scale_f32_16x16x128_f8f6f4 v[50:53], v[138:145], v[34:41], v[50:53], v172, v172 op_sel:[0,1,0] op_sel_hi:[0,0,0]
	v_mfma_scale_f32_16x16x128_f8f6f4 v[38:41], v[130:137], v[150:157], v[232:235], v172, v172 op_sel:[0,1,0] op_sel_hi:[0,0,0]
	v_mfma_scale_f32_16x16x128_f8f6f4 v[34:37], v[138:145], v[150:157], v[236:239], v172, v172 op_sel:[0,1,0] op_sel_hi:[0,0,0]
	v_mfma_scale_f32_16x16x128_f8f6f4 v[22:25], v[130:137], v[158:165], v[240:243], v172, v172 op_sel:[0,1,0] op_sel_hi:[0,0,0]
	v_mfma_scale_f32_16x16x128_f8f6f4 v[18:21], v[138:145], v[158:165], v[244:247], v172, v172 op_sel:[0,1,0] op_sel_hi:[0,0,0]
	v_mfma_scale_f32_16x16x128_f8f6f4 v[6:9], v[130:137], v[176:183], v[248:251], v172, v172 op_sel:[0,1,0] op_sel_hi:[0,0,0]
	v_mfma_scale_f32_16x16x128_f8f6f4 v[2:5], v[138:145], v[176:183], v[146:149], v172, v172 op_sel:[0,1,0] op_sel_hi:[0,0,0]
	s_setprio 0
	s_barrier
	s_add_i32 s49, s49, 2
	s_addk_i32 s4, 0x100
	s_addk_i32 s5, 0x100
	s_cmp_gt_u32 s49, 13
	s_cbranch_scc0 .LBB0_1725
	s_and_b64 vcc, exec, s[10:11]
	s_cbranch_vccz .LBB0_1728
	s_barrier
